# speedup vs baseline: 1.0061x; 1.0061x over previous
_Z11jacobi_mainPKfS0_S0_PyPf:
	s_lshl_b32 s3, s2, 3
	s_load_dwordx4 s[12:15], s[0:1], 0x0
	s_load_dwordx2 s[4:5], s[0:1], 0x10
	s_and_b32 s3, s3, 56
	s_ashr_i32 s33, s2, 5
	v_readfirstlane_b32 s40, v0
	s_add_i32 s18, s3, s33
	s_bfe_u32 s3, s2, 0x20003
	s_lshl_b32 s7, s3, 8
	s_and_b32 s10, s40, 0xffffffc0
	s_ashr_i32 s19, s18, 31
	s_lshr_b32 s34, s2, 3
	s_add_i32 s11, s10, s7
	s_lshl_b64 s[8:9], s[18:19], 22
	v_and_b32_e32 v206, 63, v0
	s_waitcnt lgkmcnt(0)
	s_add_u32 s8, s12, s8
	s_addc_u32 s9, s13, s9
	v_or_b32_e32 v154, s11, v206
	s_lshl_b32 s6, s18, 10
	v_add_u32_e32 v2, s6, v154
	v_ashrrev_i32_e32 v3, 31, v2
	v_lshlrev_b64 v[2:3], 2, v[2:3]
	v_lshl_add_u64 v[4:5], s[14:15], 0, v[2:3]
	global_load_dword v1, v[4:5], off
	s_movk_i32 s12, 0x1004
	v_mov_b64_e32 v[4:5], s[8:9]
	v_mad_i64_i32 v[4:5], s[12:13], v154, s12, v[4:5]
	v_lshl_add_u64 v[2:3], s[4:5], 0, v[2:3]
	global_load_dword v207, v[4:5], off
	global_load_dword v66, v[2:3], off
	s_lshl_b32 s76, s6, 2
	s_add_u32 s76, s4, s76
	s_addc_u32 s77, s5, 0
	v_lshlrev_b32_e32 v220, 4, v0
	global_load_dwordx4 v[224:227], v220, s[76:77]
	s_load_dwordx2 s[16:17], s[0:1], 0x20
	v_ashrrev_i32_e32 v155, 31, v154
	s_mov_b32 s21, 0
	s_lshr_b32 s35, s40, 6
	v_cmp_eq_u32_e64 s[12:13], 0, v206
	s_load_dwordx2 s[0:1], s[0:1], 0x18
	v_lshrrev_b32_e32 v67, 5, v206
	v_or_b32_e32 v132, s11, v67
	s_lshl_b64 s[14:15], s[18:19], 14
	v_ashrrev_i32_e32 v133, 31, v132
	v_and_b32_e32 v124, 31, v0
	s_waitcnt lgkmcnt(0)
	s_cmp_gt_u32 s40, 63
	s_cbranch_scc1 .Lpz_skip
	s_mul_i32 s94, s18, 0x650
	s_lshl_b32 s95, s3, 2
	s_add_u32 s94, s94, s95
	s_add_u32 s94, s16, s94
	s_addc_u32 s95, s17, 0
	v_lshlrev_b32_e32 v220, 4, v206
	v_mov_b32_e32 v221, 0
	global_store_dword v220, v221, s[94:95]
	v_cmp_gt_u32_e32 vcc, 36, v206
	s_and_saveexec_b64 s[92:93], vcc
	global_store_dword v220, v221, s[94:95] offset:1024
	s_mov_b64 exec, s[92:93]
.Lpz_skip:
	s_add_u32 s14, s0, s14
	v_lshlrev_b64 v[2:3], 12, v[132:133]
	s_addc_u32 s15, s1, s15
	s_add_i32 s0, s7, 0x100
	v_lshl_add_u64 v[2:3], s[8:9], 0, v[2:3]
	v_lshlrev_b32_e32 v190, 4, v124
	v_mov_b32_e32 v191, 0
	s_and_b32 s26, s0, 0x300
	v_lshl_add_u64 v[130:131], v[2:3], 0, v[190:191]
	s_mov_b64 s[0:1], 0x30000
	v_lshl_add_u64 v[126:127], v[130:131], 0, s[0:1]
	s_mov_b64 s[0:1], 0x32000
	v_lshl_add_u64 v[128:129], v[130:131], 0, s[0:1]
	s_mov_b64 s[0:1], 0x34000
	v_lshl_add_u64 v[134:135], v[130:131], 0, s[0:1]
	s_mov_b64 s[0:1], 0x36000
	v_lshl_add_u64 v[136:137], v[130:131], 0, s[0:1]
	s_mov_b64 s[0:1], 0x38000
	v_lshl_add_u64 v[138:139], v[130:131], 0, s[0:1]
	s_mov_b64 s[0:1], 0x3a000
	v_lshl_add_u64 v[140:141], v[130:131], 0, s[0:1]
	s_mov_b64 s[0:1], 0x3c000
	s_or_b32 s24, s7, 0x80
	v_lshl_add_u64 v[142:143], v[130:131], 0, s[0:1]
	s_mov_b64 s[0:1], 0x3e000
	s_lshl_b32 s20, s7, 2
	v_lshl_add_u64 v[144:145], v[130:131], 0, s[0:1]
	s_lshl_b32 s8, s24, 2
	s_mov_b32 s9, s21
	v_lshl_add_u64 v[2:3], v[126:127], 0, s[20:21]
	v_lshl_add_u64 v[4:5], v[128:129], 0, s[20:21]
	v_lshl_add_u64 v[6:7], v[134:135], 0, s[20:21]
	v_lshl_add_u64 v[8:9], v[136:137], 0, s[20:21]
	v_lshl_add_u64 v[10:11], v[138:139], 0, s[20:21]
	v_lshl_add_u64 v[12:13], v[140:141], 0, s[20:21]
	v_lshl_add_u64 v[14:15], v[142:143], 0, s[20:21]
	v_lshl_add_u64 v[16:17], v[144:145], 0, s[20:21]
	v_lshl_add_u64 v[18:19], v[126:127], 0, s[8:9]
	v_lshl_add_u64 v[20:21], v[128:129], 0, s[8:9]
	v_lshl_add_u64 v[22:23], v[134:135], 0, s[8:9]
	v_lshl_add_u64 v[24:25], v[136:137], 0, s[8:9]
	s_lshl_b32 s0, s26, 2
	s_mov_b32 s1, s21
	v_lshl_add_u64 v[72:73], v[138:139], 0, s[8:9]
	v_lshl_add_u64 v[102:103], v[140:141], 0, s[8:9]
	v_lshl_add_u64 v[104:105], v[142:143], 0, s[8:9]
	v_lshl_add_u64 v[106:107], v[144:145], 0, s[8:9]
	v_lshl_add_u64 v[108:109], v[126:127], 0, s[0:1]
	v_lshl_add_u64 v[110:111], v[128:129], 0, s[0:1]
	v_lshl_add_u64 v[112:113], v[134:135], 0, s[0:1]
	v_lshl_add_u64 v[114:115], v[136:137], 0, s[0:1]
	v_lshl_add_u64 v[116:117], v[138:139], 0, s[0:1]
	v_lshl_add_u64 v[118:119], v[140:141], 0, s[0:1]
	v_lshl_add_u64 v[120:121], v[142:143], 0, s[0:1]
	v_lshl_add_u64 v[122:123], v[144:145], 0, s[0:1]
	global_load_dwordx4 v[68:71], v[2:3], off nt
	global_load_dwordx4 v[78:81], v[4:5], off nt
	global_load_dwordx4 v[82:85], v[6:7], off nt
	global_load_dwordx4 v[90:93], v[8:9], off nt
	global_load_dwordx4 v[98:101], v[10:11], off nt
	global_load_dwordx4 v[62:65], v[12:13], off nt
	global_load_dwordx4 v[54:57], v[14:15], off nt
	global_load_dwordx4 v[46:49], v[16:17], off nt
	global_load_dwordx4 v[94:97], v[18:19], off nt
	global_load_dwordx4 v[86:89], v[20:21], off nt
	global_load_dwordx4 v[74:77], v[22:23], off nt
	global_load_dwordx4 v[58:61], v[24:25], off nt
	global_load_dwordx4 v[50:53], v[72:73], off nt
	global_load_dwordx4 v[42:45], v[102:103], off nt
	global_load_dwordx4 v[38:41], v[104:105], off nt
	global_load_dwordx4 v[34:37], v[106:107], off nt
	global_load_dwordx4 v[30:33], v[108:109], off nt
	global_load_dwordx4 v[26:29], v[110:111], off nt
	s_nop 0
	global_load_dwordx4 v[22:25], v[112:113], off nt
	global_load_dwordx4 v[18:21], v[114:115], off nt
	global_load_dwordx4 v[14:17], v[116:117], off nt
	global_load_dwordx4 v[10:13], v[118:119], off nt
	global_load_dwordx4 v[6:9], v[120:121], off nt
	global_load_dwordx4 v[2:5], v[122:123], off nt
	s_waitcnt vmcnt(25)
	v_div_scale_f32 v72, s[22:23], v207, v207, 1.0
	v_rcp_f32_e32 v73, v72
	s_lshl_b32 s11, s10, 2
	s_mul_i32 s19, s35, 0x1100
	s_add_i32 s22, s11, 0x26600
	v_fma_f32 v103, -v72, v73, 1.0
	v_fmac_f32_e32 v73, v103, v73
	v_div_scale_f32 v103, vcc, 1.0, v207, 1.0
	v_mul_f32_e32 v104, v103, v73
	v_fma_f32 v105, -v72, v104, v103
	v_fmac_f32_e32 v104, v105, v73
	v_fma_f32 v72, -v72, v104, v103
	v_div_fmas_f32 v72, v72, v73, v104
	v_div_fixup_f32 v72, v72, v207, 1.0
	s_waitcnt vmcnt(24)
	v_fma_f32 v208, v72, v1, -v66
	v_mbcnt_lo_u32_b32 v244, -1, 0
	v_mbcnt_hi_u32_b32 v244, -1, v244
	v_and_b32_e32 v245, 64, v244
	v_xor_b32_e32 v246, 32, v244
	v_add_u32_e32 v245, 64, v245
	v_cmp_lt_i32_e32 vcc, v246, v245
	v_xor_b32_e32 v248, 8, v244
	s_nop 0
	v_cndmask_b32_e32 v246, v244, v246, vcc
	v_lshlrev_b32_e32 v246, 2, v246
	v_mul_f32_e32 v247, v1, v1
	ds_bpermute_b32 v246, v246, v247
	v_xor_b32_e32 v247, 16, v244
	v_cmp_lt_i32_e32 vcc, v247, v245
	s_waitcnt lgkmcnt(0)
	v_fmac_f32_e32 v246, v1, v1
	v_cndmask_b32_e32 v247, v244, v247, vcc
	v_lshlrev_b32_e32 v247, 2, v247
	ds_bpermute_b32 v247, v247, v246
	v_cmp_lt_i32_e32 vcc, v248, v245
	s_waitcnt lgkmcnt(0)
	v_add_f32_e32 v246, v246, v247
	v_cndmask_b32_e32 v248, v244, v248, vcc
	v_lshlrev_b32_e32 v248, 2, v248
	ds_bpermute_b32 v247, v248, v246
	v_xor_b32_e32 v248, 4, v244
	v_cmp_lt_i32_e32 vcc, v248, v245
	s_waitcnt lgkmcnt(0)
	v_add_f32_e32 v246, v246, v247
	v_cndmask_b32_e32 v248, v244, v248, vcc
	v_lshlrev_b32_e32 v248, 2, v248
	ds_bpermute_b32 v247, v248, v246
	v_xor_b32_e32 v248, 2, v244
	v_cmp_lt_i32_e32 vcc, v248, v245
	s_waitcnt lgkmcnt(0)
	v_add_f32_e32 v246, v246, v247
	v_cndmask_b32_e32 v248, v244, v248, vcc
	v_lshlrev_b32_e32 v248, 2, v248
	ds_bpermute_b32 v247, v248, v246
	v_xor_b32_e32 v248, 1, v244
	v_cmp_lt_i32_e32 vcc, v248, v245
	s_nop 1
	v_cndmask_b32_e32 v245, v244, v248, vcc
	s_waitcnt lgkmcnt(0)
	v_add_f32_e32 v244, v246, v247
	v_lshlrev_b32_e32 v245, 2, v245
	ds_bpermute_b32 v245, v245, v244
	s_and_saveexec_b64 s[80:81], s[12:13]
	s_cbranch_execz .LBB0_2
	s_lshl_b32 s82, s35, 2
	s_add_i32 s82, s82, 0x26a00
	s_waitcnt lgkmcnt(0)
	v_add_f32_e32 v244, v244, v245
	v_mov_b32_e32 v245, s82
	ds_write_b32 v245, v244

.Lj_stop:
	s_branch .LBB0_45
